# k_gcn gather loop diet (plain index loads + select, fma_mix accumulate), L1 hazard nops filled with o-gate exps; phase-3 loops left as baseline for deterministic neighbour order
# speedup vs baseline: 1.0569x; 1.0086x over previous
.LBB1_371:
	s_cmp_eq_u32 s9, 0
	s_cbranch_scc1 .LBB1_392
	s_add_i32 s6, s9, -1
	s_bitcmp1_b32 s6, 0
	s_cselect_b32 s7, 0x2800, 0
	v_add_u32_e32 v59, s7, v1
	ds_read_b128 v[60:63], v59
	ds_read_b128 v[64:67], v59 offset:5120
	s_bitcmp1_b32 s9, 0
	s_cselect_b32 s10, 0x2800, 0
	s_cmp_eq_u32 s6, 23
	s_waitcnt lgkmcnt(1)
	v_mfma_f32_16x16x32_f16 v[70:73], v[2:5], v[60:63], v[18:21]
	v_mfma_f32_16x16x32_f16 v[74:77], v[22:25], v[60:63], v[38:41]
	v_add_u32_e32 v60, s10, v1
	ds_read_b128 v[78:81], v60 offset:20480
	ds_read_b128 v[82:85], v60 offset:25600
	s_cselect_b64 s[10:11], -1, 0
	s_waitcnt lgkmcnt(2)
	v_mfma_f32_16x16x32_f16 v[70:73], v[6:9], v[64:67], v[70:73]
	s_cmp_lg_u32 s6, 23
	v_mfma_f32_16x16x32_f16 v[62:65], v[26:29], v[64:67], v[74:77]
	s_waitcnt lgkmcnt(1)
	v_mfma_f32_16x16x32_f16 v[70:73], v[10:13], v[78:81], v[70:73]
	v_mfma_f32_16x16x32_f16 v[62:65], v[30:33], v[78:81], v[62:65]
	s_waitcnt lgkmcnt(0)
	v_mfma_f32_16x16x32_f16 v[70:73], v[14:17], v[82:85], v[70:73]
	v_mfma_f32_16x16x32_f16 v[62:65], v[34:37], v[82:85], v[62:65]
	ds_read_b128 v[86:89], v59 offset:256
	ds_read_b128 v[90:93], v59 offset:5376
	ds_read_b128 v[94:97], v60 offset:20736
	ds_read_b128 v[98:101], v60 offset:25856
	s_nop 2
	v_exp_f32_e32 v67, v72
	v_exp_f32_e32 v66, v64
	v_exp_f32_e32 v53, v70
	v_exp_f32_e32 v52, v62
	v_exp_f32_e32 v71, v71
	v_exp_f32_e32 v70, v63
	v_pk_add_f32 v[62:63], v[66:67], 1.0 op_sel_hi:[1,0]
	v_pk_fma_f32 v[66:67], v[66:67], s[8:9], v[68:69] op_sel_hi:[1,0,0]
	v_pk_fma_f32 v[52:53], v[52:53], v[62:63], v[62:63]
	v_pk_fma_f32 v[66:67], v[66:67], v[70:71], v[66:67]
	v_fma_f32 v58, v71, v53, v53
	v_fma_f32 v61, v70, v52, v52
	v_rcp_f32_e32 v63, v58
	v_rcp_f32_e32 v62, v61
	v_pk_fma_f32 v[42:43], v[42:43], v[52:53], v[66:67]
	v_exp_f32_e32 v61, v73
	v_pk_mul_f32 v[42:43], v[42:43], v[62:63]
	v_add_u32_e32 v58, s7, v54
	v_exp_f32_e32 v52, v43
	v_exp_f32_e32 v53, v42
	v_exp_f32_e32 v64, v65
	v_pk_add_f32 v[52:53], v[52:53], 1.0 op_sel_hi:[1,0]
	s_nop 0
	v_fma_f32 v61, v61, v52, v52
	v_pk_add_f32 v[62:63], v[52:53], 2.0 op_sel_hi:[1,0] neg_lo:[1,0] neg_hi:[1,0]
	v_fmac_f32_e32 v53, v64, v53
	v_rcp_f32_e32 v52, v61
	v_rcp_f32_e32 v53, v53
	s_nop 0
	v_pk_mul_f32 v[52:53], v[62:63], v[52:53]
	s_nop 0
	v_cvt_pk_f16_f32 v61, v52, v53
	ds_write_b32 v58, v61 offset:20480
	s_cbranch_scc0 .Lxt_0
.LBB1_376:
	s_andn2_b64 vcc, exec, s[10:11]
	s_waitcnt lgkmcnt(1)
	v_mfma_f32_16x16x32_f16 v[74:77], v[2:5], v[86:89], v[18:21]
	v_mfma_f32_16x16x32_f16 v[62:65], v[22:25], v[86:89], v[38:41]
	v_mfma_f32_16x16x32_f16 v[74:77], v[6:9], v[90:93], v[74:77]
	v_mfma_f32_16x16x32_f16 v[62:65], v[26:29], v[90:93], v[62:65]
	v_mfma_f32_16x16x32_f16 v[74:77], v[10:13], v[94:97], v[74:77]
	v_mfma_f32_16x16x32_f16 v[62:65], v[30:33], v[94:97], v[62:65]
	v_mfma_f32_16x16x32_f16 v[74:77], v[14:17], v[98:101], v[74:77]
	v_mfma_f32_16x16x32_f16 v[62:65], v[34:37], v[98:101], v[62:65]
	ds_read_b128 v[102:105], v59 offset:512
	ds_read_b128 v[106:109], v59 offset:5632
	ds_read_b128 v[110:113], v60 offset:20992
	ds_read_b128 v[114:117], v60 offset:26112
	s_nop 2
	v_exp_f32_e32 v67, v76
	v_exp_f32_e32 v66, v64
	v_exp_f32_e32 v53, v74
	v_exp_f32_e32 v52, v62
	v_exp_f32_e32 v71, v75
	v_exp_f32_e32 v70, v63
	v_pk_add_f32 v[62:63], v[66:67], 1.0 op_sel_hi:[1,0]
	v_pk_fma_f32 v[66:67], v[66:67], s[8:9], v[68:69] op_sel_hi:[1,0,0]
	v_pk_fma_f32 v[52:53], v[52:53], v[62:63], v[62:63]
	v_pk_fma_f32 v[66:67], v[66:67], v[70:71], v[66:67]
	v_fma_f32 v61, v71, v53, v53
	v_rcp_f32_e32 v63, v61
	v_fma_f32 v61, v70, v52, v52
	v_rcp_f32_e32 v62, v61
	v_pk_fma_f32 v[44:45], v[44:45], v[52:53], v[66:67]
	v_pk_mul_f32 v[44:45], v[44:45], v[62:63]
	v_exp_f32_e32 v61, v77
	v_exp_f32_e32 v52, v45
	v_exp_f32_e32 v53, v44
	v_exp_f32_e32 v64, v65
	v_pk_add_f32 v[52:53], v[52:53], 1.0 op_sel_hi:[1,0]
	s_nop 0
	v_fma_f32 v61, v61, v52, v52
	v_pk_add_f32 v[62:63], v[52:53], 2.0 op_sel_hi:[1,0] neg_lo:[1,0] neg_hi:[1,0]
	v_fmac_f32_e32 v53, v64, v53
	v_rcp_f32_e32 v52, v61
	v_rcp_f32_e32 v53, v53
	v_cndmask_b32_e64 v61, 0, 1, s[10:11]
	v_cmp_ne_u32_e64 s[6:7], 1, v61
	v_pk_mul_f32 v[52:53], v[62:63], v[52:53]
	s_nop 0
	v_cvt_pk_f16_f32 v61, v52, v53
	ds_write_b32 v58, v61 offset:20736
	s_cbranch_vccz .Lxt_1
.LBB1_380:
	s_and_b64 vcc, exec, s[6:7]
	s_waitcnt lgkmcnt(1)
	v_mfma_f32_16x16x32_f16 v[74:77], v[2:5], v[102:105], v[18:21]
	v_mfma_f32_16x16x32_f16 v[62:65], v[22:25], v[102:105], v[38:41]
	v_mfma_f32_16x16x32_f16 v[74:77], v[6:9], v[106:109], v[74:77]
	v_mfma_f32_16x16x32_f16 v[62:65], v[26:29], v[106:109], v[62:65]
	v_mfma_f32_16x16x32_f16 v[74:77], v[10:13], v[110:113], v[74:77]
	v_mfma_f32_16x16x32_f16 v[62:65], v[30:33], v[110:113], v[62:65]
	v_mfma_f32_16x16x32_f16 v[74:77], v[14:17], v[114:117], v[74:77]
	v_mfma_f32_16x16x32_f16 v[62:65], v[34:37], v[114:117], v[62:65]
	ds_read_b128 v[86:89], v59 offset:768
	ds_read_b128 v[90:93], v59 offset:5888
	ds_read_b128 v[94:97], v60 offset:21248
	ds_read_b128 v[98:101], v60 offset:26368
	s_nop 2
	v_exp_f32_e32 v67, v76
	v_exp_f32_e32 v66, v64
	v_exp_f32_e32 v53, v74
	v_exp_f32_e32 v52, v62
	v_exp_f32_e32 v71, v75
	v_exp_f32_e32 v70, v63
	v_pk_add_f32 v[62:63], v[66:67], 1.0 op_sel_hi:[1,0]
	v_pk_fma_f32 v[66:67], v[66:67], s[8:9], v[68:69] op_sel_hi:[1,0,0]
	v_pk_fma_f32 v[52:53], v[52:53], v[62:63], v[62:63]
	v_pk_fma_f32 v[66:67], v[66:67], v[70:71], v[66:67]
	v_fma_f32 v61, v71, v53, v53
	v_rcp_f32_e32 v63, v61
	v_fma_f32 v61, v70, v52, v52
	v_rcp_f32_e32 v62, v61
	v_pk_fma_f32 v[46:47], v[46:47], v[52:53], v[66:67]
	v_pk_mul_f32 v[46:47], v[46:47], v[62:63]
	v_exp_f32_e32 v61, v77
	v_exp_f32_e32 v52, v47
	v_exp_f32_e32 v53, v46
	v_exp_f32_e32 v64, v65
	v_pk_add_f32 v[52:53], v[52:53], 1.0 op_sel_hi:[1,0]
	s_nop 0
	v_fma_f32 v61, v61, v52, v52
	v_pk_add_f32 v[62:63], v[52:53], 2.0 op_sel_hi:[1,0] neg_lo:[1,0] neg_hi:[1,0]
	v_fmac_f32_e32 v53, v64, v53
	v_rcp_f32_e32 v52, v61
	v_rcp_f32_e32 v53, v53
	s_nop 0
	v_pk_mul_f32 v[52:53], v[62:63], v[52:53]
	s_nop 0
	v_cvt_pk_f16_f32 v61, v52, v53
	ds_write_b32 v58, v61 offset:20992
	s_cbranch_vccz .Lxt_2
.LBB1_384:
	s_and_b64 vcc, exec, s[6:7]
	s_waitcnt lgkmcnt(1)
	v_mfma_f32_16x16x32_f16 v[74:77], v[2:5], v[86:89], v[18:21]
	v_mfma_f32_16x16x32_f16 v[62:65], v[22:25], v[86:89], v[38:41]
	v_mfma_f32_16x16x32_f16 v[74:77], v[6:9], v[90:93], v[74:77]
	v_mfma_f32_16x16x32_f16 v[62:65], v[26:29], v[90:93], v[62:65]
	v_mfma_f32_16x16x32_f16 v[74:77], v[10:13], v[94:97], v[74:77]
	v_mfma_f32_16x16x32_f16 v[62:65], v[30:33], v[94:97], v[62:65]
	v_mfma_f32_16x16x32_f16 v[74:77], v[14:17], v[98:101], v[74:77]
	v_mfma_f32_16x16x32_f16 v[62:65], v[34:37], v[98:101], v[62:65]
	ds_read_b128 v[102:105], v59 offset:1024
	ds_read_b128 v[106:109], v59 offset:6144
	ds_read_b128 v[110:113], v60 offset:21504
	ds_read_b128 v[114:117], v60 offset:26624
	s_nop 2
	v_exp_f32_e32 v67, v76
	v_exp_f32_e32 v66, v64
	v_exp_f32_e32 v53, v74
	v_exp_f32_e32 v52, v62
	v_exp_f32_e32 v71, v75
	v_exp_f32_e32 v70, v63
	v_pk_add_f32 v[62:63], v[66:67], 1.0 op_sel_hi:[1,0]
	v_pk_fma_f32 v[66:67], v[66:67], s[8:9], v[68:69] op_sel_hi:[1,0,0]
	v_pk_fma_f32 v[52:53], v[52:53], v[62:63], v[62:63]
	v_pk_fma_f32 v[66:67], v[66:67], v[70:71], v[66:67]
	v_fma_f32 v61, v71, v53, v53
	v_rcp_f32_e32 v63, v61
	v_fma_f32 v61, v70, v52, v52
	v_rcp_f32_e32 v62, v61
	v_pk_fma_f32 v[48:49], v[48:49], v[52:53], v[66:67]
	v_pk_mul_f32 v[48:49], v[48:49], v[62:63]
	v_exp_f32_e32 v61, v77
	v_exp_f32_e32 v52, v49
	v_exp_f32_e32 v53, v48
	v_exp_f32_e32 v64, v65
	v_pk_add_f32 v[52:53], v[52:53], 1.0 op_sel_hi:[1,0]
	s_nop 0
	v_fma_f32 v61, v61, v52, v52
	v_pk_add_f32 v[62:63], v[52:53], 2.0 op_sel_hi:[1,0] neg_lo:[1,0] neg_hi:[1,0]
	v_fmac_f32_e32 v53, v64, v53
	v_rcp_f32_e32 v52, v61
	v_rcp_f32_e32 v53, v53
	s_nop 0
	v_pk_mul_f32 v[52:53], v[62:63], v[52:53]
	s_nop 0
	v_cvt_pk_f16_f32 v61, v52, v53
	ds_write_b32 v58, v61 offset:21248
	s_cbranch_vccz .Lxt_3
.LBB1_388:
	s_and_b64 vcc, exec, s[6:7]
	s_waitcnt lgkmcnt(1)
	v_mfma_f32_16x16x32_f16 v[74:77], v[2:5], v[102:105], v[18:21]
	v_mfma_f32_16x16x32_f16 v[60:63], v[22:25], v[102:105], v[38:41]
	v_mfma_f32_16x16x32_f16 v[74:77], v[6:9], v[106:109], v[74:77]
	v_mfma_f32_16x16x32_f16 v[60:63], v[26:29], v[106:109], v[60:63]
	v_mfma_f32_16x16x32_f16 v[74:77], v[10:13], v[110:113], v[74:77]
	v_mfma_f32_16x16x32_f16 v[60:63], v[30:33], v[110:113], v[60:63]
	v_mfma_f32_16x16x32_f16 v[74:77], v[14:17], v[114:117], v[74:77]
	v_mfma_f32_16x16x32_f16 v[60:63], v[34:37], v[114:117], v[60:63]
	s_nop 6
	v_exp_f32_e32 v65, v76
	v_exp_f32_e32 v64, v62
	v_exp_f32_e32 v53, v74
	v_exp_f32_e32 v52, v60
	v_exp_f32_e32 v67, v75
	v_exp_f32_e32 v66, v61
	v_pk_add_f32 v[60:61], v[64:65], 1.0 op_sel_hi:[1,0]
	v_pk_fma_f32 v[64:65], v[64:65], s[8:9], v[68:69] op_sel_hi:[1,0,0]
	v_pk_fma_f32 v[52:53], v[52:53], v[60:61], v[60:61]
	v_pk_fma_f32 v[64:65], v[64:65], v[66:67], v[64:65]
	v_fma_f32 v59, v67, v53, v53
	v_rcp_f32_e32 v61, v59
	v_fma_f32 v59, v66, v52, v52
	v_rcp_f32_e32 v60, v59
	v_pk_fma_f32 v[50:51], v[50:51], v[52:53], v[64:65]
	v_pk_mul_f32 v[50:51], v[50:51], v[60:61]
	v_exp_f32_e32 v59, v77
	v_exp_f32_e32 v52, v51
	v_exp_f32_e32 v53, v50
	v_exp_f32_e32 v62, v63
	v_pk_add_f32 v[52:53], v[52:53], 1.0 op_sel_hi:[1,0]
	s_nop 0
	v_fma_f32 v59, v59, v52, v52
	v_pk_add_f32 v[60:61], v[52:53], 2.0 op_sel_hi:[1,0] neg_lo:[1,0] neg_hi:[1,0]
	v_fmac_f32_e32 v53, v62, v53
	v_rcp_f32_e32 v52, v59
	v_rcp_f32_e32 v53, v53
	s_nop 0
	v_pk_mul_f32 v[52:53], v[60:61], v[52:53]
	s_nop 0
	v_cvt_pk_f16_f32 v59, v52, v53
	ds_write_b32 v58, v59 offset:21504
	s_cbranch_vccz .Lxt_4

.LBB2_8:
	s_or_b64 exec, exec, s[4:5]
	v_and_b32_e32 v82, 15, v0
	v_or_b32_e32 v51, s6, v83
	v_add_u32_e32 v34, s29, v51
	v_lshlrev_b32_e32 v54, 4, v82
	s_mov_b32 s27, 0x20000
	s_mov_b32 s26, 0x4e2100
	s_waitcnt lgkmcnt(0)
	s_and_b32 s25, s25, 0xffff
	v_lshl_or_b32 v35, v34, 8, v54
	buffer_load_dwordx4 v[64:67], v35, s[24:27], 0 offen
	v_ashrrev_i32_e32 v35, 31, v34
	v_lshl_add_u64 v[34:35], v[34:35], 2, s[2:3]
	global_load_dword v52, v[34:35], off
	v_mbcnt_lo_u32_b32 v34, -1, 0
	v_mbcnt_hi_u32_b32 v34, -1, v34
	v_and_b32_e32 v37, 64, v34
	v_xor_b32_e32 v35, 32, v34
	v_add_u32_e32 v37, 64, v37
	v_cmp_lt_i32_e32 vcc, v35, v37
	v_xor_b32_e32 v39, 16, v34
	s_load_dwordx2 s[2:3], s[0:1], 0x78
	s_load_dwordx8 s[4:11], s[0:1], 0x58
	s_load_dwordx8 s[12:19], s[0:1], 0x38
	v_cndmask_b32_e32 v35, v34, v35, vcc
	v_lshlrev_b32_e32 v84, 2, v35
	ds_bpermute_b32 v35, v84, v53
	v_cmp_lt_i32_e32 vcc, v39, v37
	s_mov_b32 s33, 4
	s_waitcnt vmcnt(1)
	v_cvt_f32_f16_e32 v62, v64
	v_cndmask_b32_e32 v34, v34, v39, vcc
	v_lshlrev_b32_e32 v85, 2, v34
	s_waitcnt lgkmcnt(0)
	v_max_i32_e32 v34, v53, v35
	ds_bpermute_b32 v35, v85, v34
	v_cvt_f32_f16_sdwa v63, v64 dst_sel:DWORD dst_unused:UNUSED_PAD src0_sel:WORD_1
	v_cvt_f32_f16_e32 v60, v65
	v_cvt_f32_f16_sdwa v61, v65 dst_sel:DWORD dst_unused:UNUSED_PAD src0_sel:WORD_1
	v_cvt_f32_f16_e32 v58, v66
	v_cvt_f32_f16_sdwa v59, v66 dst_sel:DWORD dst_unused:UNUSED_PAD src0_sel:WORD_1
	v_cvt_f32_f16_e32 v56, v67
	v_cvt_f32_f16_sdwa v57, v67 dst_sel:DWORD dst_unused:UNUSED_PAD src0_sel:WORD_1
	s_waitcnt lgkmcnt(0)
	v_max_i32_e32 v34, v34, v35
	s_nop 0
	v_readfirstlane_b32 s31, v34
	v_mov_b32_e32 v70, 0x4e20
	s_cmp_lt_i32 s31, 1
	s_cbranch_scc1 .LBB2_19
.LBB2_9:
	v_add_lshl_u32 v68, v50, s33, 2
	v_subrev_u32_e32 v69, s33, v53
	global_load_dword v64, v68, s[22:23]
	global_load_dword v55, v68, s[22:23] offset:4
	global_load_dword v66, v68, s[22:23] offset:8
	global_load_dword v65, v68, s[22:23] offset:12
	v_lshl_or_b32 v34, v36, 8, v54
	buffer_load_dwordx4 v[34:37], v34, s[24:27], 0 offen
	v_lshl_or_b32 v38, v38, 8, v54
	buffer_load_dwordx4 v[38:41], v38, s[24:27], 0 offen
	v_lshl_or_b32 v42, v42, 8, v54
	buffer_load_dwordx4 v[42:45], v42, s[24:27], 0 offen
	v_lshl_or_b32 v46, v46, 8, v54
	buffer_load_dwordx4 v[46:49], v46, s[24:27], 0 offen
	s_add_i32 s20, s33, 4
	s_cmp_ge_i32 s33, s31
	s_waitcnt vmcnt(3)
	v_fma_mix_f32 v62, v34, 1.0, v62 op_sel_hi:[1,0,0]
	v_fma_mix_f32 v63, v34, 1.0, v63 op_sel:[1,0,0] op_sel_hi:[1,0,0]
	v_fma_mix_f32 v60, v35, 1.0, v60 op_sel_hi:[1,0,0]
	v_fma_mix_f32 v61, v35, 1.0, v61 op_sel:[1,0,0] op_sel_hi:[1,0,0]
	v_fma_mix_f32 v58, v36, 1.0, v58 op_sel_hi:[1,0,0]
	v_fma_mix_f32 v59, v36, 1.0, v59 op_sel:[1,0,0] op_sel_hi:[1,0,0]
	v_fma_mix_f32 v56, v37, 1.0, v56 op_sel_hi:[1,0,0]
	v_fma_mix_f32 v57, v37, 1.0, v57 op_sel:[1,0,0] op_sel_hi:[1,0,0]
	s_waitcnt vmcnt(2)
	v_fma_mix_f32 v62, v38, 1.0, v62 op_sel_hi:[1,0,0]
	v_fma_mix_f32 v63, v38, 1.0, v63 op_sel:[1,0,0] op_sel_hi:[1,0,0]
	v_fma_mix_f32 v60, v39, 1.0, v60 op_sel_hi:[1,0,0]
	v_fma_mix_f32 v61, v39, 1.0, v61 op_sel:[1,0,0] op_sel_hi:[1,0,0]
	v_fma_mix_f32 v58, v40, 1.0, v58 op_sel_hi:[1,0,0]
	v_fma_mix_f32 v59, v40, 1.0, v59 op_sel:[1,0,0] op_sel_hi:[1,0,0]
	v_fma_mix_f32 v56, v41, 1.0, v56 op_sel_hi:[1,0,0]
	v_fma_mix_f32 v57, v41, 1.0, v57 op_sel:[1,0,0] op_sel_hi:[1,0,0]
	s_waitcnt vmcnt(1)
	v_fma_mix_f32 v62, v42, 1.0, v62 op_sel_hi:[1,0,0]
	v_fma_mix_f32 v63, v42, 1.0, v63 op_sel:[1,0,0] op_sel_hi:[1,0,0]
	v_fma_mix_f32 v60, v43, 1.0, v60 op_sel_hi:[1,0,0]
	v_fma_mix_f32 v61, v43, 1.0, v61 op_sel:[1,0,0] op_sel_hi:[1,0,0]
	v_fma_mix_f32 v58, v44, 1.0, v58 op_sel_hi:[1,0,0]
	v_fma_mix_f32 v59, v44, 1.0, v59 op_sel:[1,0,0] op_sel_hi:[1,0,0]
	v_fma_mix_f32 v56, v45, 1.0, v56 op_sel_hi:[1,0,0]
	v_fma_mix_f32 v57, v45, 1.0, v57 op_sel:[1,0,0] op_sel_hi:[1,0,0]
	s_waitcnt vmcnt(0)
	v_fma_mix_f32 v62, v46, 1.0, v62 op_sel_hi:[1,0,0]
	v_fma_mix_f32 v63, v46, 1.0, v63 op_sel:[1,0,0] op_sel_hi:[1,0,0]
	v_fma_mix_f32 v60, v47, 1.0, v60 op_sel_hi:[1,0,0]
	v_fma_mix_f32 v61, v47, 1.0, v61 op_sel:[1,0,0] op_sel_hi:[1,0,0]
	v_fma_mix_f32 v58, v48, 1.0, v58 op_sel_hi:[1,0,0]
	v_fma_mix_f32 v59, v48, 1.0, v59 op_sel:[1,0,0] op_sel_hi:[1,0,0]
	v_fma_mix_f32 v56, v49, 1.0, v56 op_sel_hi:[1,0,0]
	v_fma_mix_f32 v57, v49, 1.0, v57 op_sel:[1,0,0] op_sel_hi:[1,0,0]
	s_cbranch_scc1 .LBB2_19
	v_cmp_lt_i32_e64 s[34:35], 0, v69
	v_cmp_lt_i32_e64 s[36:37], 1, v69
	v_cmp_lt_i32_e64 s[38:39], 2, v69
	v_cmp_lt_i32_e64 s[40:41], 3, v69
	s_mov_b32 s33, s20
	v_cndmask_b32_e64 v36, v70, v64, s[34:35]
	v_cndmask_b32_e64 v38, v70, v55, s[36:37]
	v_cndmask_b32_e64 v42, v70, v66, s[38:39]
	v_cndmask_b32_e64 v46, v70, v65, s[40:41]
	s_branch .LBB2_9

	.amdhsa_kernel _Z5k_gcnILi128ELb1ELi16EEvPKDv8_DF16_PKiS4_PKfS2_S6_PDF16_S6_S6_S2_S6_S2_S6_S6_S6_PfS4_
		.amdhsa_group_segment_fixed_size 12288
		.amdhsa_private_segment_fixed_size 0
		.amdhsa_kernarg_size 136
		.amdhsa_user_sgpr_count 2
		.amdhsa_user_sgpr_dispatch_ptr 0
		.amdhsa_user_sgpr_queue_ptr 0
		.amdhsa_user_sgpr_kernarg_segment_ptr 1
		.amdhsa_user_sgpr_dispatch_id 0
		.amdhsa_user_sgpr_kernarg_preload_length 0
		.amdhsa_user_sgpr_kernarg_preload_offset 0
		.amdhsa_user_sgpr_private_segment_size 0
		.amdhsa_uses_dynamic_stack 0
		.amdhsa_enable_private_segment 0
		.amdhsa_system_sgpr_workgroup_id_x 1
		.amdhsa_system_sgpr_workgroup_id_y 0
		.amdhsa_system_sgpr_workgroup_id_z 0
		.amdhsa_system_sgpr_workgroup_info 0
		.amdhsa_system_vgpr_workitem_id 0
		.amdhsa_next_free_vgpr 96
		.amdhsa_next_free_sgpr 42
		.amdhsa_accum_offset 96
		.amdhsa_reserve_vcc 1
		.amdhsa_float_round_mode_32 0
		.amdhsa_float_round_mode_16_64 0
		.amdhsa_float_denorm_mode_32 3
		.amdhsa_float_denorm_mode_16_64 3
		.amdhsa_dx10_clamp 1
		.amdhsa_ieee_mode 1
		.amdhsa_fp16_overflow 0
		.amdhsa_tg_split 0
		.amdhsa_exception_fp_ieee_invalid_op 0
		.amdhsa_exception_fp_denorm_src 0
		.amdhsa_exception_fp_ieee_div_zero 0
		.amdhsa_exception_fp_ieee_overflow 0
		.amdhsa_exception_fp_ieee_underflow 0
		.amdhsa_exception_fp_ieee_inexact 0
		.amdhsa_exception_int_div_zero 0
	.end_amdhsa_kernel

amdhsa.kernels:
  - .agpr_count:     0
    .args:
      - .actual_access:  read_only
        .address_space:  global
        .offset:         0
        .size:           8
        .value_kind:     global_buffer
      - .actual_access:  read_only
        .address_space:  global
        .offset:         8
        .size:           8
        .value_kind:     global_buffer
      - .actual_access:  read_only
        .address_space:  global
        .offset:         16
        .size:           8
        .value_kind:     global_buffer
      - .actual_access:  read_only
        .address_space:  global
        .offset:         24
        .size:           8
        .value_kind:     global_buffer
      - .actual_access:  read_only
        .address_space:  global
        .offset:         32
        .size:           8
        .value_kind:     global_buffer
      - .actual_access:  read_only
        .address_space:  global
        .offset:         40
        .size:           8
        .value_kind:     global_buffer
      - .actual_access:  read_only
        .address_space:  global
        .offset:         48
        .size:           8
        .value_kind:     global_buffer
      - .actual_access:  read_only
        .address_space:  global
        .offset:         56
        .size:           8
        .value_kind:     global_buffer
      - .actual_access:  write_only
        .address_space:  global
        .offset:         64
        .size:           8
        .value_kind:     global_buffer
      - .actual_access:  write_only
        .address_space:  global
        .offset:         72
        .size:           8
        .value_kind:     global_buffer
      - .actual_access:  write_only
        .address_space:  global
        .offset:         80
        .size:           8
        .value_kind:     global_buffer
      - .actual_access:  write_only
        .address_space:  global
        .offset:         88
        .size:           8
        .value_kind:     global_buffer
      - .address_space:  global
        .offset:         96
        .size:           8
        .value_kind:     global_buffer
      - .address_space:  global
        .offset:         104
        .size:           8
        .value_kind:     global_buffer
      - .address_space:  global
        .offset:         112
        .size:           8
        .value_kind:     global_buffer
      - .address_space:  global
        .offset:         120
        .size:           8
        .value_kind:     global_buffer
      - .actual_access:  read_only
        .address_space:  global
        .offset:         128
        .size:           8
        .value_kind:     global_buffer
      - .actual_access:  write_only
        .address_space:  global
        .offset:         136
        .size:           8
        .value_kind:     global_buffer
    .group_segment_fixed_size: 84096
    .kernarg_segment_align: 8
    .kernarg_segment_size: 144
    .language:       OpenCL C
    .language_version:
      - 2
      - 0
    .max_flat_workgroup_size: 1024
    .name:           _Z14k_csr_fallbackPKiS0_S0_PKfS2_S2_S2_S2_PDv8_DF16_S4_S4_S4_PiS5_PfS4_S2_PDF16_
    .private_segment_fixed_size: 0
    .sgpr_count:     50
    .sgpr_spill_count: 0
    .symbol:         _Z14k_csr_fallbackPKiS0_S0_PKfS2_S2_S2_S2_PDv8_DF16_S4_S4_S4_PiS5_PfS4_S2_PDF16_.kd
    .uniform_work_group_size: 1
    .uses_dynamic_stack: false
    .vgpr_count:     93
    .vgpr_spill_count: 0
    .wavefront_size: 64
  - .agpr_count:     0
    .args:
      - .actual_access:  read_only
        .address_space:  global
        .offset:         0
        .size:           8
        .value_kind:     global_buffer
      - .actual_access:  read_only
        .address_space:  global
        .offset:         8
        .size:           8
        .value_kind:     global_buffer
      - .actual_access:  read_only
        .address_space:  global
        .offset:         16
        .size:           8
        .value_kind:     global_buffer
      - .actual_access:  read_only
        .address_space:  global
        .offset:         24
        .size:           8
        .value_kind:     global_buffer
      - .actual_access:  read_only
        .address_space:  global
        .offset:         32
        .size:           8
        .value_kind:     global_buffer
      - .actual_access:  read_only
        .address_space:  global
        .offset:         40
        .size:           8
        .value_kind:     global_buffer
      - .actual_access:  read_only
        .address_space:  global
        .offset:         48
        .size:           8
        .value_kind:     global_buffer
      - .actual_access:  read_only
        .address_space:  global
        .offset:         56
        .size:           8
        .value_kind:     global_buffer
      - .actual_access:  read_only
        .address_space:  global
        .offset:         64
        .size:           8
        .value_kind:     global_buffer
      - .actual_access:  write_only
        .address_space:  global
        .offset:         72
        .size:           8
        .value_kind:     global_buffer
      - .offset:         80
        .size:           152
        .value_kind:     by_value
      - .offset:         232
        .size:           4
        .value_kind:     hidden_block_count_x
      - .offset:         236
        .size:           4
        .value_kind:     hidden_block_count_y
      - .offset:         240
        .size:           4
        .value_kind:     hidden_block_count_z
      - .offset:         244
        .size:           2
        .value_kind:     hidden_group_size_x
      - .offset:         246
        .size:           2
        .value_kind:     hidden_group_size_y
      - .offset:         248
        .size:           2
        .value_kind:     hidden_group_size_z
      - .offset:         250
        .size:           2
        .value_kind:     hidden_remainder_x
      - .offset:         252
        .size:           2
        .value_kind:     hidden_remainder_y
      - .offset:         254
        .size:           2
        .value_kind:     hidden_remainder_z
      - .offset:         272
        .size:           8
        .value_kind:     hidden_global_offset_x
      - .offset:         280
        .size:           8
        .value_kind:     hidden_global_offset_y
      - .offset:         288
        .size:           8
        .value_kind:     hidden_global_offset_z
      - .offset:         296
        .size:           2
        .value_kind:     hidden_grid_dims
    .group_segment_fixed_size: 134696
    .kernarg_segment_align: 8
    .kernarg_segment_size: 488
    .language:       OpenCL C
    .language_version:
      - 2
      - 0
    .max_flat_workgroup_size: 1024
    .name:           _Z11k_lstm_mfmaPKfS0_S0_S0_S0_S0_S0_S0_S0_Pf6WkArgs
    .private_segment_fixed_size: 0
    .sgpr_count:     76
    .sgpr_spill_count: 0
    .symbol:         _Z11k_lstm_mfmaPKfS0_S0_S0_S0_S0_S0_S0_S0_Pf6WkArgs.kd
    .uniform_work_group_size: 1
    .uses_dynamic_stack: false
    .vgpr_count:     118
    .vgpr_spill_count: 0
    .wavefront_size: 64
  - .agpr_count:     0
    .args:
      - .actual_access:  read_only
        .address_space:  global
        .offset:         0
        .size:           8
        .value_kind:     global_buffer
      - .actual_access:  read_only
        .address_space:  global
        .offset:         8
        .size:           8
        .value_kind:     global_buffer
      - .actual_access:  read_only
        .address_space:  global
        .offset:         16
        .size:           8
        .value_kind:     global_buffer
      - .actual_access:  read_only
        .address_space:  global
        .offset:         24
        .size:           8
        .value_kind:     global_buffer
      - .actual_access:  read_only
        .address_space:  global
        .offset:         32
        .size:           8
        .value_kind:     global_buffer
      - .actual_access:  read_only
        .address_space:  global
        .offset:         40
        .size:           8
        .value_kind:     global_buffer
      - .actual_access:  read_only
        .address_space:  global
        .offset:         48
        .size:           8
        .value_kind:     global_buffer
      - .actual_access:  read_only
        .address_space:  global
        .offset:         56
        .size:           8
        .value_kind:     global_buffer
      - .actual_access:  read_only
        .address_space:  global
        .offset:         64
        .size:           8
        .value_kind:     global_buffer
      - .actual_access:  read_only
        .address_space:  global
        .offset:         72
        .size:           8
        .value_kind:     global_buffer
      - .actual_access:  read_only
        .address_space:  global
        .offset:         80
        .size:           8
        .value_kind:     global_buffer
      - .actual_access:  read_only
        .address_space:  global
        .offset:         88
        .size:           8
        .value_kind:     global_buffer
      - .actual_access:  read_only
        .address_space:  global
        .offset:         96
        .size:           8
        .value_kind:     global_buffer
      - .actual_access:  read_only
        .address_space:  global
        .offset:         104
        .size:           8
        .value_kind:     global_buffer
      - .actual_access:  read_only
        .address_space:  global
        .offset:         112
        .size:           8
        .value_kind:     global_buffer
      - .actual_access:  write_only
        .address_space:  global
        .offset:         120
        .size:           8
        .value_kind:     global_buffer
      - .actual_access:  read_only
        .address_space:  global
        .offset:         128
        .size:           8
        .value_kind:     global_buffer
    .group_segment_fixed_size: 12288
    .kernarg_segment_align: 8
    .kernarg_segment_size: 136
    .language:       OpenCL C
    .language_version:
      - 2
      - 0
    .max_flat_workgroup_size: 256
    .name:           _Z5k_gcnILi128ELb1ELi16EEvPKDv8_DF16_PKiS4_PKfS2_S6_PDF16_S6_S6_S2_S6_S2_S6_S6_S6_PfS4_
    .private_segment_fixed_size: 0
    .sgpr_count:     48
    .sgpr_spill_count: 0
    .symbol:         _Z5k_gcnILi128ELb1ELi16EEvPKDv8_DF16_PKiS4_PKfS2_S6_PDF16_S6_S6_S2_S6_S2_S6_S6_S6_PfS4_.kd
    .uniform_work_group_size: 1
    .uses_dynamic_stack: false
    .vgpr_count:     96
    .vgpr_spill_count: 0
    .wavefront_size: 64
